# speedup vs baseline: 1.0206x; 1.0097x over previous
.LBB0_18:
	ds_read_b128 v[0:3], v41
	ds_read_b128 v[4:7], v42
	ds_read_b128 v[8:11], v43
	ds_read_b128 v[12:15], v44
	v_add_u32_e32 v45, s6, v136
	v_mad_u64_u32 v[16:17], s[6:7], v45, s9, v[134:135]
	v_lshl_add_u32 v16, v16, 6, v135
	v_add_u32_e32 v137, v16, v34
	v_add_u32_e32 v150, v16, v35
	v_add_u32_e32 v151, v16, v37
	v_add_u32_e32 v152, v16, v38
	v_add_u32_e32 v153, v16, v39
	v_add_u32_e32 v154, v16, v36
	v_add_u32_e32 v16, 0x880, v16
	v_add_u32_e32 v155, v16, v34
	v_add_u32_e32 v156, v16, v35
	v_add_u32_e32 v157, v16, v37
	v_add_u32_e32 v158, v16, v38
	v_add_u32_e32 v159, v16, v39
	v_add_u32_e32 v160, v16, v36
	ds_read_b128 v[46:49], v137 offset:1024
	ds_read_b128 v[122:125], v150 offset:1024
	ds_read_b128 v[126:129], v151 offset:1088
	ds_read_b128 v[130:133], v152 offset:1088
	ds_read_b128 v[138:141], v153 offset:1152
	ds_read_b128 v[142:145], v154 offset:1152
	ds_read_b128 v[146:149], v137 offset:3200
	s_waitcnt lgkmcnt(6)
	v_mfma_f32_32x32x16_f16 v[16:31], v[114:117], v[46:49], v[0:15]
	s_waitcnt lgkmcnt(5)
	v_mfma_f32_32x32x16_f16 v[16:31], v[50:53], v[122:125], v[16:31]
	ds_read_b128 v[46:49], v150 offset:3200
	s_waitcnt lgkmcnt(5)
	v_mfma_f32_32x32x16_f16 v[16:31], v[54:57], v[126:129], v[16:31]
	ds_read_b128 v[122:125], v151 offset:3264
	s_waitcnt lgkmcnt(5)
	v_mfma_f32_32x32x16_f16 v[16:31], v[58:61], v[130:133], v[16:31]
	ds_read_b128 v[126:129], v152 offset:3264
	s_waitcnt lgkmcnt(5)
	v_mfma_f32_32x32x16_f16 v[16:31], v[62:65], v[138:141], v[16:31]
	ds_read_b128 v[130:133], v153 offset:3328
	s_waitcnt lgkmcnt(5)
	v_mfma_f32_32x32x16_f16 v[16:31], v[66:69], v[142:145], v[16:31]
	ds_read_b128 v[138:141], v154 offset:3328
	s_waitcnt lgkmcnt(5)
	v_mfma_f32_32x32x16_f16 v[16:31], v[70:73], v[146:149], v[16:31]
	ds_read_b128 v[142:145], v137 offset:5376
	s_waitcnt lgkmcnt(5)
	v_mfma_f32_32x32x16_f16 v[16:31], v[74:77], v[46:49], v[16:31]
	ds_read_b128 v[146:149], v150 offset:5376
	s_waitcnt lgkmcnt(5)
	v_mfma_f32_32x32x16_f16 v[16:31], v[78:81], v[122:125], v[16:31]
	ds_read_b128 v[46:49], v151 offset:5440
	s_waitcnt lgkmcnt(5)
	v_mfma_f32_32x32x16_f16 v[16:31], v[82:85], v[126:129], v[16:31]
	ds_read_b128 v[122:125], v152 offset:5440
	s_waitcnt lgkmcnt(5)
	v_mfma_f32_32x32x16_f16 v[16:31], v[86:89], v[130:133], v[16:31]
	ds_read_b128 v[126:129], v153 offset:5504
	s_waitcnt lgkmcnt(5)
	v_mfma_f32_32x32x16_f16 v[16:31], v[90:93], v[138:141], v[16:31]
	ds_read_b128 v[130:133], v154 offset:5504
	s_waitcnt lgkmcnt(5)
	v_mfma_f32_32x32x16_f16 v[16:31], v[94:97], v[142:145], v[16:31]
	ds_read_b128 v[138:141], v155 offset:1024
	s_waitcnt lgkmcnt(5)
	v_mfma_f32_32x32x16_f16 v[16:31], v[98:101], v[146:149], v[16:31]
	ds_read_b128 v[142:145], v156 offset:1024
	s_waitcnt lgkmcnt(5)
	v_mfma_f32_32x32x16_f16 v[16:31], v[102:105], v[46:49], v[16:31]
	ds_read_b128 v[146:149], v157 offset:1088
	s_waitcnt lgkmcnt(5)
	v_mfma_f32_32x32x16_f16 v[16:31], v[106:109], v[122:125], v[16:31]
	ds_read_b128 v[46:49], v158 offset:1088
	s_waitcnt lgkmcnt(5)
	v_mfma_f32_32x32x16_f16 v[16:31], v[110:113], v[126:129], v[16:31]
	ds_read_b128 v[122:125], v159 offset:1152
	s_waitcnt lgkmcnt(5)
	v_mfma_f32_32x32x16_f16 v[16:31], v[118:121], v[130:133], v[16:31]
	ds_read_b128 v[126:129], v160 offset:1152
	s_waitcnt lgkmcnt(5)
	v_mfma_f32_32x32x16_f16 v[0:15], v[114:117], v[138:141], v[0:15]
	ds_read_b128 v[130:133], v155 offset:3200
	s_waitcnt lgkmcnt(5)
	v_mfma_f32_32x32x16_f16 v[0:15], v[50:53], v[142:145], v[0:15]
	ds_read_b128 v[138:141], v156 offset:3200
	s_waitcnt lgkmcnt(5)
	v_mfma_f32_32x32x16_f16 v[0:15], v[54:57], v[146:149], v[0:15]
	ds_read_b128 v[142:145], v157 offset:3264
	s_waitcnt lgkmcnt(5)
	v_mfma_f32_32x32x16_f16 v[0:15], v[58:61], v[46:49], v[0:15]
	ds_read_b128 v[146:149], v158 offset:3264
	s_waitcnt lgkmcnt(5)
	v_mfma_f32_32x32x16_f16 v[0:15], v[62:65], v[122:125], v[0:15]
	ds_read_b128 v[46:49], v159 offset:3328
	s_waitcnt lgkmcnt(5)
	v_mfma_f32_32x32x16_f16 v[0:15], v[66:69], v[126:129], v[0:15]
	ds_read_b128 v[122:125], v160 offset:3328
	s_waitcnt lgkmcnt(5)
	v_mfma_f32_32x32x16_f16 v[0:15], v[70:73], v[130:133], v[0:15]
	ds_read_b128 v[126:129], v155 offset:5376
	s_waitcnt lgkmcnt(5)
	v_mfma_f32_32x32x16_f16 v[0:15], v[74:77], v[138:141], v[0:15]
	ds_read_b128 v[130:133], v156 offset:5376
	s_waitcnt lgkmcnt(5)
	v_mfma_f32_32x32x16_f16 v[0:15], v[78:81], v[142:145], v[0:15]
	ds_read_b128 v[138:141], v157 offset:5440
	s_waitcnt lgkmcnt(5)
	v_mfma_f32_32x32x16_f16 v[0:15], v[82:85], v[146:149], v[0:15]
	ds_read_b128 v[142:145], v158 offset:5440
	s_waitcnt lgkmcnt(5)
	v_mfma_f32_32x32x16_f16 v[0:15], v[86:89], v[46:49], v[0:15]
	ds_read_b128 v[146:149], v159 offset:5504
	s_waitcnt lgkmcnt(5)
	v_mfma_f32_32x32x16_f16 v[0:15], v[90:93], v[122:125], v[0:15]
	ds_read_b128 v[46:49], v160 offset:5504
	s_waitcnt lgkmcnt(5)
	v_mfma_f32_32x32x16_f16 v[0:15], v[94:97], v[126:129], v[0:15]
	s_waitcnt lgkmcnt(4)
	v_mfma_f32_32x32x16_f16 v[0:15], v[98:101], v[130:133], v[0:15]
	s_waitcnt lgkmcnt(3)
	v_mfma_f32_32x32x16_f16 v[0:15], v[102:105], v[138:141], v[0:15]
	s_waitcnt lgkmcnt(2)
	v_mfma_f32_32x32x16_f16 v[0:15], v[106:109], v[142:145], v[0:15]
	s_waitcnt lgkmcnt(1)
	v_mfma_f32_32x32x16_f16 v[0:15], v[110:113], v[146:149], v[0:15]
	s_waitcnt lgkmcnt(0)
	v_mfma_f32_32x32x16_f16 v[0:15], v[118:121], v[46:49], v[0:15]
	s_nop 11
	v_cvt_pk_f16_f32 v2, v2, v3
	v_cvt_pk_f16_f32 v3, v4, v5
	v_cvt_pk_f16_f32 v5, v6, v7
	v_cvt_pk_f16_f32 v6, v24, v25
	v_cvt_pk_f16_f32 v7, v8, v9
	v_cvt_pk_f16_f32 v0, v0, v1
	v_cvt_pk_f16_f32 v1, v18, v19
	v_pk_max_f16 v6, v6, v7
	v_cvt_pk_f16_f32 v7, v26, v27
	v_cvt_pk_f16_f32 v8, v10, v11
	v_pk_max_f16 v1, v1, v2
	v_cvt_pk_f16_f32 v2, v20, v21
	v_pk_max_f16 v7, v7, v8
	v_cvt_pk_f16_f32 v8, v28, v29
	v_cvt_pk_f16_f32 v9, v12, v13
	v_cvt_pk_f16_f32 v16, v16, v17
	v_pk_max_f16 v2, v2, v3
	v_cvt_pk_f16_f32 v3, v22, v23
	v_pk_max_f16 v8, v8, v9
	v_cvt_pk_f16_f32 v9, v30, v31
	v_cvt_pk_f16_f32 v12, v14, v15
	v_pk_max_f16 v0, v16, v0
	v_pk_max_f16 v3, v3, v5
	v_pk_max_f16 v9, v9, v12
	v_mov_b32_dpp v16, v0 quad_perm:[1,0,3,2] row_mask:0xf bank_mask:0xf bound_ctrl:1
	v_mov_b32_dpp v17, v1 quad_perm:[1,0,3,2] row_mask:0xf bank_mask:0xf bound_ctrl:1
	v_mov_b32_dpp v4, v2 quad_perm:[1,0,3,2] row_mask:0xf bank_mask:0xf bound_ctrl:1
	v_mov_b32_dpp v5, v3 quad_perm:[1,0,3,2] row_mask:0xf bank_mask:0xf bound_ctrl:1
	v_mov_b32_dpp v18, v6 quad_perm:[1,0,3,2] row_mask:0xf bank_mask:0xf bound_ctrl:1
	v_mov_b32_dpp v10, v7 quad_perm:[1,0,3,2] row_mask:0xf bank_mask:0xf bound_ctrl:1
	v_mov_b32_dpp v11, v8 quad_perm:[1,0,3,2] row_mask:0xf bank_mask:0xf bound_ctrl:1
	v_mov_b32_dpp v12, v9 quad_perm:[1,0,3,2] row_mask:0xf bank_mask:0xf bound_ctrl:1
	s_and_saveexec_b64 s[6:7], s[0:1]
	s_cbranch_execz .LBB0_17
	v_pk_max_f16 v10, v10, v10
	v_pk_max_f16 v7, v7, v7
	v_pk_max_f16 v8, v8, v8
	v_pk_max_f16 v7, v7, v10
	v_pk_max_f16 v10, v11, v11
	v_pk_max_f16 v4, v4, v4
	v_pk_max_f16 v2, v2, v2
	v_pk_max_f16 v8, v8, v10
	v_pk_max_f16 v10, v12, v12
	v_pk_max_f16 v9, v9, v9
	v_pk_max_f16 v2, v2, v4
	v_pk_max_f16 v4, v5, v5
	v_pk_max_f16 v3, v3, v3
	v_pk_max_f16 v9, v9, v10
	v_pk_max_f16 v10, v16, v16
	v_pk_max_f16 v0, v0, v0
	v_pk_max_f16 v3, v3, v4
	v_add_u32_e32 v4, s8, v45
	v_pk_max_f16 v0, v0, v10
	v_pk_max_f16 v10, v17, v17
	v_pk_max_f16 v1, v1, v1
	v_lshl_add_u32 v4, v4, 11, v40
	v_pk_max_f16 v13, v18, v18
	v_pk_max_f16 v6, v6, v6
	v_pk_max_f16 v1, v1, v10
	v_ashrrev_i32_e32 v5, 31, v4
	v_pk_max_f16 v6, v6, v13
	v_pk_max_f16 v0, v0, 0
	v_pk_max_f16 v1, v1, 0
	v_pk_max_f16 v2, v2, 0
	v_pk_max_f16 v3, v3, 0
	v_lshl_add_u64 v[4:5], v[4:5], 1, v[32:33]
	v_pk_max_f16 v6, v6, 0
	v_pk_max_f16 v7, v7, 0
	v_pk_max_f16 v8, v8, 0
	v_pk_max_f16 v9, v9, 0
	global_store_dwordx4 v[4:5], v[0:3], off sc0 sc1
	global_store_dwordx4 v[4:5], v[6:9], off offset:16 sc0 sc1
	s_branch .LBB0_17
